# v23 + row_scale_table fast path in all four phases that build the table (w1, G_in l=0/1, KVQ/Q): 256 rstd computed once per workgroup with 8 loads per thread on waves 0-3, same summation tree
# baseline (speedup 1.0000x reference)
.LBB0_450:
	s_ashr_i32 s11, s10, 31
	s_waitcnt vmcnt(0)
	s_cmp_lg_u32 s33, 0x100
	s_cbranch_scc1 .Lrst_hg0_slow
	v_cmp_gt_u32_e32 vcc, 0x100, v0
	s_and_saveexec_b64 s[0:1], vcc
	s_cbranch_execz .Lrst_hg0_done
	s_and_b32 s4, s10, 7
	s_lshl_b32 s4, s4, 2
	s_bfe_u32 s26, s10, 0x20003
	s_or_b32 s4, s4, s26
	s_lshl_b32 s4, s4, 15
	s_add_u32 s26, s82, 0x36300000
	s_addc_u32 s27, s83, 0
	s_add_u32 s26, s26, s4
	s_addc_u32 s27, s27, 0
	v_lshlrev_b32_e32 v2, 7, v0
	global_load_dwordx4 v[4:7], v2, s[26:27]
	global_load_dwordx4 v[8:11], v2, s[26:27] offset:16
	global_load_dwordx4 v[12:15], v2, s[26:27] offset:32
	global_load_dwordx4 v[16:19], v2, s[26:27] offset:48
	global_load_dwordx4 v[20:23], v2, s[26:27] offset:64
	global_load_dwordx4 v[24:27], v2, s[26:27] offset:80
	global_load_dwordx4 v[28:31], v2, s[26:27] offset:96
	global_load_dwordx4 v[32:35], v2, s[26:27] offset:112
	v_readlane_b32 s4, v255, 4
	v_mov_b32_e32 v36, 0x358637bd
	s_waitcnt vmcnt(0)
	v_pk_add_f32 v[4:5], v[4:5], v[8:9]
	v_pk_add_f32 v[6:7], v[6:7], v[10:11]
	v_pk_add_f32 v[12:13], v[12:13], v[16:17]
	v_pk_add_f32 v[14:15], v[14:15], v[18:19]
	v_pk_add_f32 v[20:21], v[20:21], v[24:25]
	v_pk_add_f32 v[22:23], v[22:23], v[26:27]
	v_pk_add_f32 v[28:29], v[28:29], v[32:33]
	v_pk_add_f32 v[30:31], v[30:31], v[34:35]
	v_pk_add_f32 v[4:5], v[4:5], v[12:13]
	v_pk_add_f32 v[6:7], v[6:7], v[14:15]
	v_pk_add_f32 v[20:21], v[20:21], v[28:29]
	v_pk_add_f32 v[22:23], v[22:23], v[30:31]
	v_pk_add_f32 v[4:5], v[4:5], v[20:21]
	v_pk_add_f32 v[6:7], v[6:7], v[22:23]
	s_nop 0
	v_add_f32_e32 v4, v5, v4
	v_add_f32_e32 v6, v6, v7
	v_add_f32_e32 v4, v4, v6
	v_fmamk_f32 v4, v4, 0x3a000000, v36
	v_rsq_f32_e32 v4, v4
	v_lshl_add_u32 v3, v0, 2, s4
	s_nop 0
	ds_write_b32 v3, v4
	ds_write_b32 v3, v4 offset:1024
	ds_write_b32 v3, v4 offset:2048
	ds_write_b32 v3, v4 offset:3072

.Lrst_hg0_slow:
	v_ashrrev_i32_e32 v34, 8, v1
	v_mov_b64_e32 v[2:3], s[10:11]
	v_mad_i64_i32 v[2:3], s[0:1], v34, s33, v[2:3]
	s_mov_b64 s[0:1], 0x400
	s_nop 0
	v_cmp_gt_i64_e32 vcc, s[0:1], v[2:3]
	v_mov_b32_e32 v37, 0
	s_and_saveexec_b64 s[26:27], vcc
	s_cbranch_execz .LBB0_456
	v_ashrrev_i32_e32 v3, 31, v2
	v_lshrrev_b32_e32 v3, 29, v3
	v_add_u32_e32 v3, v2, v3
	v_and_b32_e32 v4, -8, v3
	v_sub_u32_e32 v4, v2, v4
	v_cmp_lt_i32_e64 s[0:1], -1, v4
	s_and_saveexec_b64 s[4:5], s[0:1]
	s_xor_b64 s[0:1], exec, s[4:5]
	v_lshlrev_b32_e32 v2, 7, v4
	s_andn2_saveexec_b64 s[0:1], s[0:1]
	v_lshl_add_u32 v2, v4, 7, v4
	s_or_b64 exec, exec, s[0:1]
	v_ashrrev_i32_e32 v3, 3, v3
	v_add_u32_e32 v2, v2, v3
	v_ashrrev_i32_e32 v3, 31, v2
	v_lshrrev_b32_e32 v3, 25, v3
	v_add_u32_e32 v3, v2, v3
	v_ashrrev_i32_e32 v4, 7, v3
	v_lshlrev_b32_e32 v4, 2, v4
	v_sub_u32_e32 v5, 32, v4
	v_min_i32_e32 v5, 4, v5
	s_waitcnt lgkmcnt(3)
	v_sub_u32_e32 v6, 0, v5
	v_max_i32_e32 v5, v5, v6
	v_cvt_f32_u32_e32 v6, v5
	v_and_b32_e32 v3, 0xffffff80, v3
	v_sub_u32_e32 v2, v2, v3
	s_waitcnt lgkmcnt(2)
	v_sub_u32_e32 v7, 0, v2
	v_rcp_iflag_f32_e32 v6, v6
	v_ashrrev_i32_e32 v3, 31, v2
	v_max_i32_e32 v2, v2, v7
	v_sub_u32_e32 v7, 0, v5
	v_mul_f32_e32 v6, 0x4f7ffffe, v6
	v_cvt_u32_f32_e32 v6, v6
	v_mul_lo_u32 v7, v7, v6
	v_mul_hi_u32 v7, v6, v7
	v_add_u32_e32 v6, v6, v7
	v_mul_hi_u32 v6, v2, v6
	v_mul_lo_u32 v6, v6, v5
	v_sub_u32_e32 v2, v2, v6
	v_sub_u32_e32 v6, v2, v5
	v_cmp_ge_u32_e64 s[0:1], v2, v5
	s_nop 1
	v_cndmask_b32_e64 v2, v2, v6, s[0:1]
	v_sub_u32_e32 v6, v2, v5
	v_cmp_ge_u32_e64 s[0:1], v2, v5
	s_nop 1
	v_cndmask_b32_e64 v2, v2, v6, s[0:1]
	v_xor_b32_e32 v2, v2, v3
	v_sub_u32_e32 v2, v2, v3
	v_add_u32_e32 v37, v4, v2
